# speedup vs baseline: 1.0383x; 1.0284x over previous
.LBB0_4:
	s_load_dwordx4 s[8:11], s[0:1], 0x10
	s_load_dwordx2 s[12:13], s[0:1], 0x20
	s_load_dwordx2 s[16:17], s[0:1], 0x8
	s_load_dwordx4 s[20:23], s[0:1], 0x30
	s_load_dwordx2 s[24:25], s[0:1], 0x40
	v_readfirstlane_b32 s26, v0
	s_lshr_b32 s26, s26, 6
	s_and_b32 s27, s4, 0xfffffff3
	s_lshl_b32 s28, s4, 1
	s_and_b32 s28, s28, 8
	s_lshr_b32 s29, s4, 1
	s_and_b32 s29, s29, 4
	s_or_b32 s27, s27, s28
	s_or_b32 s27, s27, s29
	s_lshl_b32 s27, s27, 2
	s_lshr_b32 s30, s4, 4
	s_and_b32 s31, s4, 15
	v_lshlrev_b32_e32 v8, 2, v0
	v_lshlrev_b32_e32 v1, 10, v0
	v_add_u32_e32 v1, s27, v1
	v_and_b32_e32 v2, 0xf3, v0
	v_lshlrev_b32_e32 v3, 1, v0
	v_and_b32_e32 v3, 8, v3
	v_lshrrev_b32_e32 v6, 1, v0
	v_and_b32_e32 v6, 4, v6
	v_or3_b32 v2, v2, v3, v6
	s_lshl_b32 s32, s4, 10
	v_lshl_add_u32 v2, v2, 2, s32
	v_and_b32_e32 v9, 63, v0
	v_lshrrev_b32_e32 v10, 4, v9
	v_and_b32_e32 v11, 15, v9
	v_lshlrev_b32_e32 v10, 10, v10
	v_lshl_or_b32 v13, v11, 2, v10
	v_and_b32_e32 v12, 3, v11
	v_lshlrev_b32_e32 v14, 1, v11
	v_and_b32_e32 v14, 8, v14
	v_lshrrev_b32_e32 v15, 1, v11
	v_and_b32_e32 v15, 4, v15
	v_or3_b32 v12, v12, v14, v15
	v_lshl_or_b32 v12, v12, 2, v10
	v_lshlrev_b32_e32 v3, 2, v9
	s_waitcnt lgkmcnt(0)
	global_load_dword v4, v1, s[10:11]
	global_load_dword v5, v8, s[8:9]
	global_load_dword v7, v2, s[12:13]
	s_lshl_b32 s33, s26, 16
	s_lshl_b32 s34, s30, 6
	s_add_u32 s34, s34, s33
	s_add_u32 s36, s10, s34
	s_addc_u32 s37, s11, 0
	s_lshl_b32 s35, s31, 6
	s_add_u32 s35, s35, s33
	s_add_u32 s38, s16, s35
	s_addc_u32 s39, s17, 0
	global_load_dword v16, v12, s[36:37]
	global_load_dword v32, v13, s[38:39]
	s_add_u32 s36, s36, 0x1000
	s_addc_u32 s37, s37, 0
	s_add_u32 s38, s38, 0x1000
	s_addc_u32 s39, s39, 0
	global_load_dword v17, v12, s[36:37]
	global_load_dword v33, v13, s[38:39]
	s_add_u32 s36, s36, 0x1000
	s_addc_u32 s37, s37, 0
	s_add_u32 s38, s38, 0x1000
	s_addc_u32 s39, s39, 0
	global_load_dword v18, v12, s[36:37]
	global_load_dword v34, v13, s[38:39]
	s_add_u32 s36, s36, 0x1000
	s_addc_u32 s37, s37, 0
	s_add_u32 s38, s38, 0x1000
	s_addc_u32 s39, s39, 0
	global_load_dword v19, v12, s[36:37]
	global_load_dword v35, v13, s[38:39]
	s_add_u32 s36, s36, 0x1000
	s_addc_u32 s37, s37, 0
	s_add_u32 s38, s38, 0x1000
	s_addc_u32 s39, s39, 0
	global_load_dword v20, v12, s[36:37]
	global_load_dword v36, v13, s[38:39]
	s_add_u32 s36, s36, 0x1000
	s_addc_u32 s37, s37, 0
	s_add_u32 s38, s38, 0x1000
	s_addc_u32 s39, s39, 0
	global_load_dword v21, v12, s[36:37]
	global_load_dword v37, v13, s[38:39]
	s_add_u32 s36, s36, 0x1000
	s_addc_u32 s37, s37, 0
	s_add_u32 s38, s38, 0x1000
	s_addc_u32 s39, s39, 0
	global_load_dword v22, v12, s[36:37]
	global_load_dword v38, v13, s[38:39]
	s_add_u32 s36, s36, 0x1000
	s_addc_u32 s37, s37, 0
	s_add_u32 s38, s38, 0x1000
	s_addc_u32 s39, s39, 0
	global_load_dword v23, v12, s[36:37]
	global_load_dword v39, v13, s[38:39]
	s_add_u32 s36, s36, 0x1000
	s_addc_u32 s37, s37, 0
	s_add_u32 s38, s38, 0x1000
	s_addc_u32 s39, s39, 0
	global_load_dword v24, v12, s[36:37]
	global_load_dword v40, v13, s[38:39]
	s_add_u32 s36, s36, 0x1000
	s_addc_u32 s37, s37, 0
	s_add_u32 s38, s38, 0x1000
	s_addc_u32 s39, s39, 0
	global_load_dword v25, v12, s[36:37]
	global_load_dword v41, v13, s[38:39]
	s_add_u32 s36, s36, 0x1000
	s_addc_u32 s37, s37, 0
	s_add_u32 s38, s38, 0x1000
	s_addc_u32 s39, s39, 0
	global_load_dword v26, v12, s[36:37]
	global_load_dword v42, v13, s[38:39]
	s_add_u32 s36, s36, 0x1000
	s_addc_u32 s37, s37, 0
	s_add_u32 s38, s38, 0x1000
	s_addc_u32 s39, s39, 0
	global_load_dword v27, v12, s[36:37]
	global_load_dword v43, v13, s[38:39]
	s_add_u32 s36, s36, 0x1000
	s_addc_u32 s37, s37, 0
	s_add_u32 s38, s38, 0x1000
	s_addc_u32 s39, s39, 0
	global_load_dword v28, v12, s[36:37]
	global_load_dword v44, v13, s[38:39]
	s_add_u32 s36, s36, 0x1000
	s_addc_u32 s37, s37, 0
	s_add_u32 s38, s38, 0x1000
	s_addc_u32 s39, s39, 0
	global_load_dword v29, v12, s[36:37]
	global_load_dword v45, v13, s[38:39]
	s_add_u32 s36, s36, 0x1000
	s_addc_u32 s37, s37, 0
	s_add_u32 s38, s38, 0x1000
	s_addc_u32 s39, s39, 0
	global_load_dword v30, v12, s[36:37]
	global_load_dword v46, v13, s[38:39]
	s_add_u32 s36, s36, 0x1000
	s_addc_u32 s37, s37, 0
	s_add_u32 s38, s38, 0x1000
	s_addc_u32 s39, s39, 0
	global_load_dword v31, v12, s[36:37]
	global_load_dword v47, v13, s[38:39]
	s_waitcnt vmcnt(32)
	v_mul_f32_e32 v6, v4, v5
	v_xor_b32_e32 v14, 0x80, v3
	ds_bpermute_b32 v15, v14, v6
	s_waitcnt lgkmcnt(0)
	v_fmac_f32_e32 v15, v4, v5
	v_mov_b32_e32 v6, v15
	v_xor_b32_e32 v14, 0x40, v3
	ds_bpermute_b32 v15, v14, v6
	s_waitcnt lgkmcnt(0)
	v_add_f32_e32 v6, v6, v15
	v_xor_b32_e32 v14, 0x20, v3
	ds_bpermute_b32 v15, v14, v6
	s_waitcnt lgkmcnt(0)
	v_add_f32_e32 v6, v6, v15
	v_xor_b32_e32 v14, 0x10, v3
	ds_bpermute_b32 v15, v14, v6
	s_waitcnt lgkmcnt(0)
	v_add_f32_e32 v6, v6, v15
	v_xor_b32_e32 v14, 0x8, v3
	ds_bpermute_b32 v15, v14, v6
	s_waitcnt lgkmcnt(0)
	v_add_f32_e32 v6, v6, v15
	v_xor_b32_e32 v14, 0x4, v3
	ds_bpermute_b32 v15, v14, v6
	s_waitcnt lgkmcnt(0)
	v_add_f32_e32 v6, v6, v15
	s_lshl_b32 s33, s26, 2
	v_mov_b32_e32 v14, s33
	ds_write_b32 v14, v6 offset:21504
	s_waitcnt vmcnt(30)
	v_mfma_f32_16x16x4_f32 v[48:51], v16, v32, 0
	s_waitcnt vmcnt(28)
	v_mfma_f32_16x16x4_f32 v[48:51], v17, v33, v[48:51]
	s_waitcnt vmcnt(26)
	v_mfma_f32_16x16x4_f32 v[48:51], v18, v34, v[48:51]
	s_waitcnt vmcnt(24)
	v_mfma_f32_16x16x4_f32 v[48:51], v19, v35, v[48:51]
	s_waitcnt vmcnt(22)
	v_mfma_f32_16x16x4_f32 v[48:51], v20, v36, v[48:51]
	s_waitcnt vmcnt(20)
	v_mfma_f32_16x16x4_f32 v[48:51], v21, v37, v[48:51]
	s_waitcnt vmcnt(18)
	v_mfma_f32_16x16x4_f32 v[48:51], v22, v38, v[48:51]
	s_waitcnt vmcnt(16)
	v_mfma_f32_16x16x4_f32 v[48:51], v23, v39, v[48:51]
	s_waitcnt vmcnt(14)
	v_mfma_f32_16x16x4_f32 v[48:51], v24, v40, v[48:51]
	s_waitcnt vmcnt(12)
	v_mfma_f32_16x16x4_f32 v[48:51], v25, v41, v[48:51]
	s_waitcnt vmcnt(10)
	v_mfma_f32_16x16x4_f32 v[48:51], v26, v42, v[48:51]
	s_waitcnt vmcnt(8)
	v_mfma_f32_16x16x4_f32 v[48:51], v27, v43, v[48:51]
	s_waitcnt vmcnt(6)
	v_mfma_f32_16x16x4_f32 v[48:51], v28, v44, v[48:51]
	s_waitcnt vmcnt(4)
	v_mfma_f32_16x16x4_f32 v[48:51], v29, v45, v[48:51]
	s_waitcnt vmcnt(2)
	v_mfma_f32_16x16x4_f32 v[48:51], v30, v46, v[48:51]
	s_waitcnt vmcnt(0)
	v_mfma_f32_16x16x4_f32 v[48:51], v31, v47, v[48:51]
	s_lshl_b32 s33, s26, 10
	v_lshrrev_b32_e32 v14, 4, v9
	v_lshlrev_b32_e32 v14, 8, v14
	v_lshl_or_b32 v14, v11, 2, v14
	v_add_u32_e32 v14, s33, v14
	s_nop 10
	ds_write_b32 v14, v48 offset:16384
	ds_write_b32 v14, v49 offset:16448
	ds_write_b32 v14, v50 offset:16512
	ds_write_b32 v14, v51 offset:16576
	s_waitcnt lgkmcnt(0)
	s_barrier
	ds_read2st64_b32 v[16:17], v8 offset0:64 offset1:68
	ds_read2st64_b32 v[18:19], v8 offset0:72 offset1:76
	v_mov_b32_e32 v20, 0
	ds_read_b128 v[24:27], v20 offset:21504
	v_lshlrev_b32_e32 v1, 1, v0
	s_lshl_b32 s33, s4, 9
	v_add_u32_e32 v1, s33, v1
	v_cvt_pk_bf16_f32 v7, v7, v7
	global_store_short v1, v7, s[24:25]
	v_lshrrev_b32_e32 v2, 4, v0
	v_lshlrev_b32_e32 v2, 9, v2
	v_and_b32_e32 v21, 15, v0
	v_lshl_or_b32 v2, v21, 1, v2
	s_lshl_b32 s33, s30, 13
	s_lshl_b32 s34, s31, 5
	s_add_u32 s33, s33, s34
	v_add_u32_e32 v2, s33, v2
	s_waitcnt lgkmcnt(2)
	v_add_f32_e32 v16, v16, v17
	s_waitcnt lgkmcnt(1)
	v_add_f32_e32 v16, v16, v18
	v_add_f32_e32 v16, v16, v19
	v_mul_f32_e32 v16, 0x3db8aa3b, v16
	v_cvt_pk_bf16_f32 v16, v16, v16
	global_store_short v2, v16, s[20:21]
	s_waitcnt lgkmcnt(0)
	v_add_f32_e32 v24, v24, v25
	v_add_f32_e32 v24, v24, v26
	v_add_f32_e32 v24, v24, v27
	v_mul_f32_e32 v24, 0x3db8aa3b, v24
	s_lshl_b32 s33, s4, 2
	v_mov_b32_e32 v25, s33
	v_cmp_eq_u32_e32 vcc, 0, v0
	s_and_saveexec_b64 s[40:41], vcc
	global_store_dword v25, v24, s[22:23]
	s_endpgm
